# P1 modulate: prefetch the token's 8 x-chunks up front, unroll the 4-trip inner loop, counted vmcnt(7) waits (on top of conversion routine)
# speedup vs baseline: 1.0094x; 1.0094x over previous
.LBB0_112:
	s_mov_b32 s44, 0x1000
	s_mov_b32 s45, 0
	v_lshl_add_u64 v[144:145], v[20:21], 0, s[44:45]
	global_load_dwordx4 v[112:115], v[20:21], off offset:-1024
	global_load_dwordx4 v[116:119], v[20:21], off
	global_load_dwordx4 v[120:123], v[20:21], off offset:1024
	global_load_dwordx4 v[124:127], v[20:21], off offset:2048
	global_load_dwordx4 v[128:131], v[20:21], off offset:3072
	global_load_dwordx4 v[132:135], v[144:145], off
	global_load_dwordx4 v[136:139], v[144:145], off offset:1024
	global_load_dwordx4 v[140:143], v[144:145], off offset:2048
	v_add_u32_e32 v29, s17, v28
	v_add_u32_e32 v90, s17, v1
	v_add_u32_e32 v98, 0x10000, v29
	v_add_u32_e32 v94, 0x12000, v29
	v_add_u32_e32 v102, 0x12400, v29
	ds_read_b128 v[30:33], v90
	ds_read_b128 v[34:37], v90 offset:1024
	ds_read_b128 v[38:41], v90 offset:8192
	ds_read_b128 v[42:45], v90 offset:9216
	ds_read_b128 v[46:49], v90 offset:16384
	ds_read_b128 v[50:53], v90 offset:17408
	ds_read_b128 v[54:57], v90 offset:24576
	ds_read_b128 v[58:61], v90 offset:25600
	ds_read_b128 v[62:65], v90 offset:32768
	ds_read_b128 v[66:69], v90 offset:33792
	ds_read_b128 v[70:73], v90 offset:40960
	ds_read_b128 v[74:77], v90 offset:41984
	ds_read_b128 v[78:81], v90 offset:49152
	ds_read_b128 v[82:85], v90 offset:50176
	ds_read_b128 v[86:89], v90 offset:57344
	ds_read_b128 v[90:93], v90 offset:58368
	v_add_u32_e32 v29, 0x10400, v29
	ds_read_b128 v[94:97], v94
	ds_read_b128 v[98:101], v98
	ds_read_b128 v[102:105], v102
	ds_read_b128 v[106:109], v29
	s_waitcnt lgkmcnt(14)
	v_pk_mov_b32 v[110:111], v[30:31], v[38:39] op_sel:[1,0]
	v_mov_b32_e32 v31, v39
	v_pk_mov_b32 v[38:39], v[32:33], v[40:41] op_sel:[1,0]
	v_mov_b32_e32 v33, v41
	s_waitcnt lgkmcnt(13)
	v_pk_mov_b32 v[40:41], v[46:47], v[54:55] op_sel:[1,0]
	v_mov_b32_e32 v47, v55
	v_pk_mov_b32 v[54:55], v[48:49], v[56:57] op_sel:[1,0]
	v_mov_b32_e32 v49, v57
	s_waitcnt lgkmcnt(9)
	v_pk_mov_b32 v[56:57], v[62:63], v[70:71] op_sel:[1,0]
	v_mov_b32_e32 v63, v71
	v_pk_mov_b32 v[70:71], v[64:65], v[72:73] op_sel:[1,0]
	v_mov_b32_e32 v65, v73
	v_pk_mov_b32 v[72:73], v[34:35], v[42:43] op_sel:[1,0]
	v_mov_b32_e32 v35, v43
	v_pk_mov_b32 v[42:43], v[36:37], v[44:45] op_sel:[1,0]
	v_mov_b32_e32 v37, v45
	v_pk_mov_b32 v[44:45], v[50:51], v[58:59] op_sel:[1,0]
	v_mov_b32_e32 v51, v59
	v_pk_mov_b32 v[58:59], v[52:53], v[60:61] op_sel:[1,0]
	v_mov_b32_e32 v53, v61
	s_waitcnt lgkmcnt(8)
	v_pk_mov_b32 v[60:61], v[66:67], v[74:75] op_sel:[1,0]
	v_mov_b32_e32 v67, v75
	v_pk_mov_b32 v[74:75], v[68:69], v[76:77] op_sel:[1,0]
	v_mov_b32_e32 v69, v77
	s_addk_i32 s17, 0x800
	s_waitcnt vmcnt(7) lgkmcnt(2)
	v_pk_fma_f32 v[96:97], v[114:115], v[96:97], v[100:101]
	v_pk_fma_f32 v[94:95], v[112:113], v[94:95], v[98:99]
	v_and_b32_sdwa v5, v97, v6 dst_sel:DWORD dst_unused:UNUSED_PAD src0_sel:WORD_1 src1_sel:DWORD
	v_and_b32_sdwa v3, v95, v6 dst_sel:DWORD dst_unused:UNUSED_PAD src0_sel:WORD_1 src1_sel:DWORD
	v_and_b32_sdwa v2, v94, v6 dst_sel:DWORD dst_unused:UNUSED_PAD src0_sel:WORD_1 src1_sel:DWORD
	v_and_b32_sdwa v4, v96, v6 dst_sel:DWORD dst_unused:UNUSED_PAD src0_sel:WORD_1 src1_sel:DWORD
	v_add3_u32 v3, v95, v3, s16
	v_add3_u32 v5, v97, v5, s16
	v_add3_u32 v2, v94, v2, s16
	v_add3_u32 v4, v96, v4, s16
	v_and_b32_e32 v5, 0xffff0000, v5
	v_and_b32_e32 v29, 0xffff0000, v3
	v_or_b32_sdwa v3, v5, v4 dst_sel:DWORD dst_unused:UNUSED_PAD src0_sel:DWORD src1_sel:WORD_1
	v_or_b32_sdwa v2, v29, v2 dst_sel:DWORD dst_unused:UNUSED_PAD src0_sel:DWORD src1_sel:WORD_1
	global_store_dwordx2 v[22:23], v[2:3], off
	v_pk_mul_f32 v[30:31], v[94:95], v[30:31]
	v_pk_mul_f32 v[32:33], v[96:97], v[32:33]
	v_pk_mul_f32 v[46:47], v[94:95], v[46:47]
	v_pk_mul_f32 v[48:49], v[96:97], v[48:49]
	v_pk_mul_f32 v[88:89], v[96:97], v[88:89]
	v_pk_mul_f32 v[86:87], v[94:95], v[86:87]
	v_mul_f32_e32 v76, v95, v79
	v_mul_f32_e32 v98, v97, v81
	v_pk_fma_f32 v[30:31], v[94:95], v[110:111], v[30:31] op_sel:[1,0,0] op_sel_hi:[0,1,1]
	v_pk_fma_f32 v[40:41], v[94:95], v[40:41], v[46:47] op_sel:[1,0,0] op_sel_hi:[0,1,1]
	v_pk_fma_f32 v[32:33], v[96:97], v[38:39], v[32:33] op_sel:[1,0,0] op_sel_hi:[0,1,1]
	v_pk_fma_f32 v[38:39], v[96:97], v[54:55], v[48:49] op_sel:[1,0,0] op_sel_hi:[0,1,1]
	v_pk_mov_b32 v[54:55], v[86:87], v[88:89] op_sel:[1,0]
	v_mov_b32_e32 v87, v89
	v_pk_mul_f32 v[62:63], v[94:95], v[62:63]
	v_pk_mul_f32 v[64:65], v[96:97], v[64:65]
	v_pk_fma_f32 v[76:77], v[94:95], v[78:79], v[76:77] op_sel_hi:[1,1,0]
	v_pk_fma_f32 v[78:79], v[96:97], v[80:81], v[98:99] op_sel_hi:[1,1,0]
	v_pk_add_f32 v[30:31], v[30:31], v[32:33]
	v_pk_add_f32 v[32:33], v[40:41], v[38:39]
	v_pk_add_f32 v[40:41], v[54:55], v[86:87]
	v_pk_fma_f32 v[46:47], v[94:95], v[56:57], v[62:63] op_sel:[1,0,0] op_sel_hi:[0,1,1]
	v_pk_fma_f32 v[48:49], v[96:97], v[70:71], v[64:65] op_sel:[1,0,0] op_sel_hi:[0,1,1]
	v_mov_b32_e32 v77, v40
	v_mov_b32_e32 v79, v41
	v_pk_add_f32 v[38:39], v[46:47], v[48:49]
	v_pk_add_f32 v[26:27], v[26:27], v[30:31]
	v_pk_add_f32 v[30:31], v[76:77], v[78:79]
	v_pk_add_f32 v[24:25], v[24:25], v[32:33]
	v_pk_add_f32 v[18:19], v[18:19], v[38:39]
	v_pk_add_f32 v[16:17], v[16:17], v[30:31]
	v_lshl_add_u64 v[20:21], v[20:21], 0, s[40:41]
	s_waitcnt vmcnt(7) lgkmcnt(0)
	v_pk_fma_f32 v[4:5], v[118:119], v[104:105], v[108:109]
	v_pk_fma_f32 v[2:3], v[116:117], v[102:103], v[106:107]
	v_and_b32_sdwa v49, v5, v6 dst_sel:DWORD dst_unused:UNUSED_PAD src0_sel:WORD_1 src1_sel:DWORD
	v_and_b32_sdwa v47, v2, v6 dst_sel:DWORD dst_unused:UNUSED_PAD src0_sel:WORD_1 src1_sel:DWORD
	v_and_b32_sdwa v29, v4, v6 dst_sel:DWORD dst_unused:UNUSED_PAD src0_sel:WORD_1 src1_sel:DWORD
	v_and_b32_sdwa v54, v3, v6 dst_sel:DWORD dst_unused:UNUSED_PAD src0_sel:WORD_1 src1_sel:DWORD
	v_pk_mul_f32 v[30:31], v[2:3], v[34:35]
	v_pk_mul_f32 v[32:33], v[4:5], v[36:37]
	v_pk_mul_f32 v[34:35], v[2:3], v[50:51]
	v_pk_mul_f32 v[36:37], v[4:5], v[52:53]
	v_pk_mul_f32 v[38:39], v[2:3], v[66:67]
	v_pk_mul_f32 v[40:41], v[4:5], v[68:69]
	v_mul_f32_e32 v46, v3, v83
	v_mul_f32_e32 v48, v5, v85
	v_pk_mul_f32 v[50:51], v[4:5], v[92:93]
	v_pk_mul_f32 v[52:53], v[2:3], v[90:91]
	v_add3_u32 v47, v2, v47, s16
	v_add3_u32 v49, v5, v49, s16
	v_add3_u32 v29, v4, v29, s16
	v_add3_u32 v54, v3, v54, s16
	v_pk_fma_f32 v[30:31], v[2:3], v[72:73], v[30:31] op_sel:[1,0,0] op_sel_hi:[0,1,1]
	v_pk_fma_f32 v[32:33], v[4:5], v[42:43], v[32:33] op_sel:[1,0,0] op_sel_hi:[0,1,1]
	v_pk_fma_f32 v[34:35], v[2:3], v[44:45], v[34:35] op_sel:[1,0,0] op_sel_hi:[0,1,1]
	v_pk_fma_f32 v[36:37], v[4:5], v[58:59], v[36:37] op_sel:[1,0,0] op_sel_hi:[0,1,1]
	v_pk_fma_f32 v[38:39], v[2:3], v[60:61], v[38:39] op_sel:[1,0,0] op_sel_hi:[0,1,1]
	v_pk_fma_f32 v[40:41], v[4:5], v[74:75], v[40:41] op_sel:[1,0,0] op_sel_hi:[0,1,1]
	v_pk_fma_f32 v[2:3], v[2:3], v[82:83], v[46:47] op_sel_hi:[1,1,0]
	v_pk_fma_f32 v[4:5], v[4:5], v[84:85], v[48:49] op_sel_hi:[1,1,0]
	v_pk_mov_b32 v[42:43], v[52:53], v[50:51] op_sel:[1,0]
	v_mov_b32_e32 v53, v51
	v_and_b32_e32 v3, 0xffff0000, v49
	v_and_b32_e32 v5, 0xffff0000, v54
	v_pk_add_f32 v[30:31], v[30:31], v[32:33]
	v_pk_add_f32 v[32:33], v[34:35], v[36:37]
	v_pk_add_f32 v[36:37], v[42:43], v[52:53]
	v_pk_add_f32 v[34:35], v[38:39], v[40:41]
	v_or_b32_sdwa v39, v3, v29 dst_sel:DWORD dst_unused:UNUSED_PAD src0_sel:DWORD src1_sel:WORD_1
	v_or_b32_sdwa v38, v5, v47 dst_sel:DWORD dst_unused:UNUSED_PAD src0_sel:DWORD src1_sel:WORD_1
	v_mov_b32_e32 v3, v36
	v_mov_b32_e32 v5, v37
	v_pk_add_f32 v[2:3], v[2:3], v[4:5]
	v_pk_add_f32 v[26:27], v[26:27], v[30:31]
	v_pk_add_f32 v[24:25], v[24:25], v[32:33]
	v_pk_add_f32 v[18:19], v[18:19], v[34:35]
	global_store_dwordx2 v[22:23], v[38:39], off offset:512
	v_lshl_add_u64 v[22:23], v[22:23], 0, s[36:37]
	v_pk_add_f32 v[16:17], v[16:17], v[2:3]
	v_add_u32_e32 v29, s17, v28
	v_add_u32_e32 v90, s17, v1
	v_add_u32_e32 v98, 0x10000, v29
	v_add_u32_e32 v94, 0x12000, v29
	v_add_u32_e32 v102, 0x12400, v29
	ds_read_b128 v[30:33], v90
	ds_read_b128 v[34:37], v90 offset:1024
	ds_read_b128 v[38:41], v90 offset:8192
	ds_read_b128 v[42:45], v90 offset:9216
	ds_read_b128 v[46:49], v90 offset:16384
	ds_read_b128 v[50:53], v90 offset:17408
	ds_read_b128 v[54:57], v90 offset:24576
	ds_read_b128 v[58:61], v90 offset:25600
	ds_read_b128 v[62:65], v90 offset:32768
	ds_read_b128 v[66:69], v90 offset:33792
	ds_read_b128 v[70:73], v90 offset:40960
	ds_read_b128 v[74:77], v90 offset:41984
	ds_read_b128 v[78:81], v90 offset:49152
	ds_read_b128 v[82:85], v90 offset:50176
	ds_read_b128 v[86:89], v90 offset:57344
	ds_read_b128 v[90:93], v90 offset:58368
	v_add_u32_e32 v29, 0x10400, v29
	ds_read_b128 v[94:97], v94
	ds_read_b128 v[98:101], v98
	ds_read_b128 v[102:105], v102
	ds_read_b128 v[106:109], v29
	s_waitcnt lgkmcnt(14)
	v_pk_mov_b32 v[110:111], v[30:31], v[38:39] op_sel:[1,0]
	v_mov_b32_e32 v31, v39
	v_pk_mov_b32 v[38:39], v[32:33], v[40:41] op_sel:[1,0]
	v_mov_b32_e32 v33, v41
	s_waitcnt lgkmcnt(13)
	v_pk_mov_b32 v[40:41], v[46:47], v[54:55] op_sel:[1,0]
	v_mov_b32_e32 v47, v55
	v_pk_mov_b32 v[54:55], v[48:49], v[56:57] op_sel:[1,0]
	v_mov_b32_e32 v49, v57
	s_waitcnt lgkmcnt(9)
	v_pk_mov_b32 v[56:57], v[62:63], v[70:71] op_sel:[1,0]
	v_mov_b32_e32 v63, v71
	v_pk_mov_b32 v[70:71], v[64:65], v[72:73] op_sel:[1,0]
	v_mov_b32_e32 v65, v73
	v_pk_mov_b32 v[72:73], v[34:35], v[42:43] op_sel:[1,0]
	v_mov_b32_e32 v35, v43
	v_pk_mov_b32 v[42:43], v[36:37], v[44:45] op_sel:[1,0]
	v_mov_b32_e32 v37, v45
	v_pk_mov_b32 v[44:45], v[50:51], v[58:59] op_sel:[1,0]
	v_mov_b32_e32 v51, v59
	v_pk_mov_b32 v[58:59], v[52:53], v[60:61] op_sel:[1,0]
	v_mov_b32_e32 v53, v61
	s_waitcnt lgkmcnt(8)
	v_pk_mov_b32 v[60:61], v[66:67], v[74:75] op_sel:[1,0]
	v_mov_b32_e32 v67, v75
	v_pk_mov_b32 v[74:75], v[68:69], v[76:77] op_sel:[1,0]
	v_mov_b32_e32 v69, v77
	s_addk_i32 s17, 0x800
	s_waitcnt vmcnt(7) lgkmcnt(2)
	v_pk_fma_f32 v[96:97], v[122:123], v[96:97], v[100:101]
	v_pk_fma_f32 v[94:95], v[120:121], v[94:95], v[98:99]
	v_and_b32_sdwa v5, v97, v6 dst_sel:DWORD dst_unused:UNUSED_PAD src0_sel:WORD_1 src1_sel:DWORD
	v_and_b32_sdwa v3, v95, v6 dst_sel:DWORD dst_unused:UNUSED_PAD src0_sel:WORD_1 src1_sel:DWORD
	v_and_b32_sdwa v2, v94, v6 dst_sel:DWORD dst_unused:UNUSED_PAD src0_sel:WORD_1 src1_sel:DWORD
	v_and_b32_sdwa v4, v96, v6 dst_sel:DWORD dst_unused:UNUSED_PAD src0_sel:WORD_1 src1_sel:DWORD
	v_add3_u32 v3, v95, v3, s16
	v_add3_u32 v5, v97, v5, s16
	v_add3_u32 v2, v94, v2, s16
	v_add3_u32 v4, v96, v4, s16
	v_and_b32_e32 v5, 0xffff0000, v5
	v_and_b32_e32 v29, 0xffff0000, v3
	v_or_b32_sdwa v3, v5, v4 dst_sel:DWORD dst_unused:UNUSED_PAD src0_sel:DWORD src1_sel:WORD_1
	v_or_b32_sdwa v2, v29, v2 dst_sel:DWORD dst_unused:UNUSED_PAD src0_sel:DWORD src1_sel:WORD_1
	global_store_dwordx2 v[22:23], v[2:3], off
	v_pk_mul_f32 v[30:31], v[94:95], v[30:31]
	v_pk_mul_f32 v[32:33], v[96:97], v[32:33]
	v_pk_mul_f32 v[46:47], v[94:95], v[46:47]
	v_pk_mul_f32 v[48:49], v[96:97], v[48:49]
	v_pk_mul_f32 v[88:89], v[96:97], v[88:89]
	v_pk_mul_f32 v[86:87], v[94:95], v[86:87]
	v_mul_f32_e32 v76, v95, v79
	v_mul_f32_e32 v98, v97, v81
	v_pk_fma_f32 v[30:31], v[94:95], v[110:111], v[30:31] op_sel:[1,0,0] op_sel_hi:[0,1,1]
	v_pk_fma_f32 v[40:41], v[94:95], v[40:41], v[46:47] op_sel:[1,0,0] op_sel_hi:[0,1,1]
	v_pk_fma_f32 v[32:33], v[96:97], v[38:39], v[32:33] op_sel:[1,0,0] op_sel_hi:[0,1,1]
	v_pk_fma_f32 v[38:39], v[96:97], v[54:55], v[48:49] op_sel:[1,0,0] op_sel_hi:[0,1,1]
	v_pk_mov_b32 v[54:55], v[86:87], v[88:89] op_sel:[1,0]
	v_mov_b32_e32 v87, v89
	v_pk_mul_f32 v[62:63], v[94:95], v[62:63]
	v_pk_mul_f32 v[64:65], v[96:97], v[64:65]
	v_pk_fma_f32 v[76:77], v[94:95], v[78:79], v[76:77] op_sel_hi:[1,1,0]
	v_pk_fma_f32 v[78:79], v[96:97], v[80:81], v[98:99] op_sel_hi:[1,1,0]
	v_pk_add_f32 v[30:31], v[30:31], v[32:33]
	v_pk_add_f32 v[32:33], v[40:41], v[38:39]
	v_pk_add_f32 v[40:41], v[54:55], v[86:87]
	v_pk_fma_f32 v[46:47], v[94:95], v[56:57], v[62:63] op_sel:[1,0,0] op_sel_hi:[0,1,1]
	v_pk_fma_f32 v[48:49], v[96:97], v[70:71], v[64:65] op_sel:[1,0,0] op_sel_hi:[0,1,1]
	v_mov_b32_e32 v77, v40
	v_mov_b32_e32 v79, v41
	v_pk_add_f32 v[38:39], v[46:47], v[48:49]
	v_pk_add_f32 v[26:27], v[26:27], v[30:31]
	v_pk_add_f32 v[30:31], v[76:77], v[78:79]
	v_pk_add_f32 v[24:25], v[24:25], v[32:33]
	v_pk_add_f32 v[18:19], v[18:19], v[38:39]
	v_pk_add_f32 v[16:17], v[16:17], v[30:31]
	v_lshl_add_u64 v[20:21], v[20:21], 0, s[40:41]
	s_waitcnt vmcnt(7) lgkmcnt(0)
	v_pk_fma_f32 v[4:5], v[126:127], v[104:105], v[108:109]
	v_pk_fma_f32 v[2:3], v[124:125], v[102:103], v[106:107]
	v_and_b32_sdwa v49, v5, v6 dst_sel:DWORD dst_unused:UNUSED_PAD src0_sel:WORD_1 src1_sel:DWORD
	v_and_b32_sdwa v47, v2, v6 dst_sel:DWORD dst_unused:UNUSED_PAD src0_sel:WORD_1 src1_sel:DWORD
	v_and_b32_sdwa v29, v4, v6 dst_sel:DWORD dst_unused:UNUSED_PAD src0_sel:WORD_1 src1_sel:DWORD
	v_and_b32_sdwa v54, v3, v6 dst_sel:DWORD dst_unused:UNUSED_PAD src0_sel:WORD_1 src1_sel:DWORD
	v_pk_mul_f32 v[30:31], v[2:3], v[34:35]
	v_pk_mul_f32 v[32:33], v[4:5], v[36:37]
	v_pk_mul_f32 v[34:35], v[2:3], v[50:51]
	v_pk_mul_f32 v[36:37], v[4:5], v[52:53]
	v_pk_mul_f32 v[38:39], v[2:3], v[66:67]
	v_pk_mul_f32 v[40:41], v[4:5], v[68:69]
	v_mul_f32_e32 v46, v3, v83
	v_mul_f32_e32 v48, v5, v85
	v_pk_mul_f32 v[50:51], v[4:5], v[92:93]
	v_pk_mul_f32 v[52:53], v[2:3], v[90:91]
	v_add3_u32 v47, v2, v47, s16
	v_add3_u32 v49, v5, v49, s16
	v_add3_u32 v29, v4, v29, s16
	v_add3_u32 v54, v3, v54, s16
	v_pk_fma_f32 v[30:31], v[2:3], v[72:73], v[30:31] op_sel:[1,0,0] op_sel_hi:[0,1,1]
	v_pk_fma_f32 v[32:33], v[4:5], v[42:43], v[32:33] op_sel:[1,0,0] op_sel_hi:[0,1,1]
	v_pk_fma_f32 v[34:35], v[2:3], v[44:45], v[34:35] op_sel:[1,0,0] op_sel_hi:[0,1,1]
	v_pk_fma_f32 v[36:37], v[4:5], v[58:59], v[36:37] op_sel:[1,0,0] op_sel_hi:[0,1,1]
	v_pk_fma_f32 v[38:39], v[2:3], v[60:61], v[38:39] op_sel:[1,0,0] op_sel_hi:[0,1,1]
	v_pk_fma_f32 v[40:41], v[4:5], v[74:75], v[40:41] op_sel:[1,0,0] op_sel_hi:[0,1,1]
	v_pk_fma_f32 v[2:3], v[2:3], v[82:83], v[46:47] op_sel_hi:[1,1,0]
	v_pk_fma_f32 v[4:5], v[4:5], v[84:85], v[48:49] op_sel_hi:[1,1,0]
	v_pk_mov_b32 v[42:43], v[52:53], v[50:51] op_sel:[1,0]
	v_mov_b32_e32 v53, v51
	v_and_b32_e32 v3, 0xffff0000, v49
	v_and_b32_e32 v5, 0xffff0000, v54
	v_pk_add_f32 v[30:31], v[30:31], v[32:33]
	v_pk_add_f32 v[32:33], v[34:35], v[36:37]
	v_pk_add_f32 v[36:37], v[42:43], v[52:53]
	v_pk_add_f32 v[34:35], v[38:39], v[40:41]
	v_or_b32_sdwa v39, v3, v29 dst_sel:DWORD dst_unused:UNUSED_PAD src0_sel:DWORD src1_sel:WORD_1
	v_or_b32_sdwa v38, v5, v47 dst_sel:DWORD dst_unused:UNUSED_PAD src0_sel:DWORD src1_sel:WORD_1
	v_mov_b32_e32 v3, v36
	v_mov_b32_e32 v5, v37
	v_pk_add_f32 v[2:3], v[2:3], v[4:5]
	v_pk_add_f32 v[26:27], v[26:27], v[30:31]
	v_pk_add_f32 v[24:25], v[24:25], v[32:33]
	v_pk_add_f32 v[18:19], v[18:19], v[34:35]
	global_store_dwordx2 v[22:23], v[38:39], off offset:512
	v_lshl_add_u64 v[22:23], v[22:23], 0, s[36:37]
	v_pk_add_f32 v[16:17], v[16:17], v[2:3]
	v_add_u32_e32 v29, s17, v28
	v_add_u32_e32 v90, s17, v1
	v_add_u32_e32 v98, 0x10000, v29
	v_add_u32_e32 v94, 0x12000, v29
	v_add_u32_e32 v102, 0x12400, v29
	ds_read_b128 v[30:33], v90
	ds_read_b128 v[34:37], v90 offset:1024
	ds_read_b128 v[38:41], v90 offset:8192
	ds_read_b128 v[42:45], v90 offset:9216
	ds_read_b128 v[46:49], v90 offset:16384
	ds_read_b128 v[50:53], v90 offset:17408
	ds_read_b128 v[54:57], v90 offset:24576
	ds_read_b128 v[58:61], v90 offset:25600
	ds_read_b128 v[62:65], v90 offset:32768
	ds_read_b128 v[66:69], v90 offset:33792
	ds_read_b128 v[70:73], v90 offset:40960
	ds_read_b128 v[74:77], v90 offset:41984
	ds_read_b128 v[78:81], v90 offset:49152
	ds_read_b128 v[82:85], v90 offset:50176
	ds_read_b128 v[86:89], v90 offset:57344
	ds_read_b128 v[90:93], v90 offset:58368
	v_add_u32_e32 v29, 0x10400, v29
	ds_read_b128 v[94:97], v94
	ds_read_b128 v[98:101], v98
	ds_read_b128 v[102:105], v102
	ds_read_b128 v[106:109], v29
	s_waitcnt lgkmcnt(14)
	v_pk_mov_b32 v[110:111], v[30:31], v[38:39] op_sel:[1,0]
	v_mov_b32_e32 v31, v39
	v_pk_mov_b32 v[38:39], v[32:33], v[40:41] op_sel:[1,0]
	v_mov_b32_e32 v33, v41
	s_waitcnt lgkmcnt(13)
	v_pk_mov_b32 v[40:41], v[46:47], v[54:55] op_sel:[1,0]
	v_mov_b32_e32 v47, v55
	v_pk_mov_b32 v[54:55], v[48:49], v[56:57] op_sel:[1,0]
	v_mov_b32_e32 v49, v57
	s_waitcnt lgkmcnt(9)
	v_pk_mov_b32 v[56:57], v[62:63], v[70:71] op_sel:[1,0]
	v_mov_b32_e32 v63, v71
	v_pk_mov_b32 v[70:71], v[64:65], v[72:73] op_sel:[1,0]
	v_mov_b32_e32 v65, v73
	v_pk_mov_b32 v[72:73], v[34:35], v[42:43] op_sel:[1,0]
	v_mov_b32_e32 v35, v43
	v_pk_mov_b32 v[42:43], v[36:37], v[44:45] op_sel:[1,0]
	v_mov_b32_e32 v37, v45
	v_pk_mov_b32 v[44:45], v[50:51], v[58:59] op_sel:[1,0]
	v_mov_b32_e32 v51, v59
	v_pk_mov_b32 v[58:59], v[52:53], v[60:61] op_sel:[1,0]
	v_mov_b32_e32 v53, v61
	s_waitcnt lgkmcnt(8)
	v_pk_mov_b32 v[60:61], v[66:67], v[74:75] op_sel:[1,0]
	v_mov_b32_e32 v67, v75
	v_pk_mov_b32 v[74:75], v[68:69], v[76:77] op_sel:[1,0]
	v_mov_b32_e32 v69, v77
	s_addk_i32 s17, 0x800
	s_waitcnt vmcnt(7) lgkmcnt(2)
	v_pk_fma_f32 v[96:97], v[130:131], v[96:97], v[100:101]
	v_pk_fma_f32 v[94:95], v[128:129], v[94:95], v[98:99]
	v_and_b32_sdwa v5, v97, v6 dst_sel:DWORD dst_unused:UNUSED_PAD src0_sel:WORD_1 src1_sel:DWORD
	v_and_b32_sdwa v3, v95, v6 dst_sel:DWORD dst_unused:UNUSED_PAD src0_sel:WORD_1 src1_sel:DWORD
	v_and_b32_sdwa v2, v94, v6 dst_sel:DWORD dst_unused:UNUSED_PAD src0_sel:WORD_1 src1_sel:DWORD
	v_and_b32_sdwa v4, v96, v6 dst_sel:DWORD dst_unused:UNUSED_PAD src0_sel:WORD_1 src1_sel:DWORD
	v_add3_u32 v3, v95, v3, s16
	v_add3_u32 v5, v97, v5, s16
	v_add3_u32 v2, v94, v2, s16
	v_add3_u32 v4, v96, v4, s16
	v_and_b32_e32 v5, 0xffff0000, v5
	v_and_b32_e32 v29, 0xffff0000, v3
	v_or_b32_sdwa v3, v5, v4 dst_sel:DWORD dst_unused:UNUSED_PAD src0_sel:DWORD src1_sel:WORD_1
	v_or_b32_sdwa v2, v29, v2 dst_sel:DWORD dst_unused:UNUSED_PAD src0_sel:DWORD src1_sel:WORD_1
	global_store_dwordx2 v[22:23], v[2:3], off
	v_pk_mul_f32 v[30:31], v[94:95], v[30:31]
	v_pk_mul_f32 v[32:33], v[96:97], v[32:33]
	v_pk_mul_f32 v[46:47], v[94:95], v[46:47]
	v_pk_mul_f32 v[48:49], v[96:97], v[48:49]
	v_pk_mul_f32 v[88:89], v[96:97], v[88:89]
	v_pk_mul_f32 v[86:87], v[94:95], v[86:87]
	v_mul_f32_e32 v76, v95, v79
	v_mul_f32_e32 v98, v97, v81
	v_pk_fma_f32 v[30:31], v[94:95], v[110:111], v[30:31] op_sel:[1,0,0] op_sel_hi:[0,1,1]
	v_pk_fma_f32 v[40:41], v[94:95], v[40:41], v[46:47] op_sel:[1,0,0] op_sel_hi:[0,1,1]
	v_pk_fma_f32 v[32:33], v[96:97], v[38:39], v[32:33] op_sel:[1,0,0] op_sel_hi:[0,1,1]
	v_pk_fma_f32 v[38:39], v[96:97], v[54:55], v[48:49] op_sel:[1,0,0] op_sel_hi:[0,1,1]
	v_pk_mov_b32 v[54:55], v[86:87], v[88:89] op_sel:[1,0]
	v_mov_b32_e32 v87, v89
	v_pk_mul_f32 v[62:63], v[94:95], v[62:63]
	v_pk_mul_f32 v[64:65], v[96:97], v[64:65]
	v_pk_fma_f32 v[76:77], v[94:95], v[78:79], v[76:77] op_sel_hi:[1,1,0]
	v_pk_fma_f32 v[78:79], v[96:97], v[80:81], v[98:99] op_sel_hi:[1,1,0]
	v_pk_add_f32 v[30:31], v[30:31], v[32:33]
	v_pk_add_f32 v[32:33], v[40:41], v[38:39]
	v_pk_add_f32 v[40:41], v[54:55], v[86:87]
	v_pk_fma_f32 v[46:47], v[94:95], v[56:57], v[62:63] op_sel:[1,0,0] op_sel_hi:[0,1,1]
	v_pk_fma_f32 v[48:49], v[96:97], v[70:71], v[64:65] op_sel:[1,0,0] op_sel_hi:[0,1,1]
	v_mov_b32_e32 v77, v40
	v_mov_b32_e32 v79, v41
	v_pk_add_f32 v[38:39], v[46:47], v[48:49]
	v_pk_add_f32 v[26:27], v[26:27], v[30:31]
	v_pk_add_f32 v[30:31], v[76:77], v[78:79]
	v_pk_add_f32 v[24:25], v[24:25], v[32:33]
	v_pk_add_f32 v[18:19], v[18:19], v[38:39]
	v_pk_add_f32 v[16:17], v[16:17], v[30:31]
	v_lshl_add_u64 v[20:21], v[20:21], 0, s[40:41]
	s_waitcnt vmcnt(7) lgkmcnt(0)
	v_pk_fma_f32 v[4:5], v[134:135], v[104:105], v[108:109]
	v_pk_fma_f32 v[2:3], v[132:133], v[102:103], v[106:107]
	v_and_b32_sdwa v49, v5, v6 dst_sel:DWORD dst_unused:UNUSED_PAD src0_sel:WORD_1 src1_sel:DWORD
	v_and_b32_sdwa v47, v2, v6 dst_sel:DWORD dst_unused:UNUSED_PAD src0_sel:WORD_1 src1_sel:DWORD
	v_and_b32_sdwa v29, v4, v6 dst_sel:DWORD dst_unused:UNUSED_PAD src0_sel:WORD_1 src1_sel:DWORD
	v_and_b32_sdwa v54, v3, v6 dst_sel:DWORD dst_unused:UNUSED_PAD src0_sel:WORD_1 src1_sel:DWORD
	v_pk_mul_f32 v[30:31], v[2:3], v[34:35]
	v_pk_mul_f32 v[32:33], v[4:5], v[36:37]
	v_pk_mul_f32 v[34:35], v[2:3], v[50:51]
	v_pk_mul_f32 v[36:37], v[4:5], v[52:53]
	v_pk_mul_f32 v[38:39], v[2:3], v[66:67]
	v_pk_mul_f32 v[40:41], v[4:5], v[68:69]
	v_mul_f32_e32 v46, v3, v83
	v_mul_f32_e32 v48, v5, v85
	v_pk_mul_f32 v[50:51], v[4:5], v[92:93]
	v_pk_mul_f32 v[52:53], v[2:3], v[90:91]
	v_add3_u32 v47, v2, v47, s16
	v_add3_u32 v49, v5, v49, s16
	v_add3_u32 v29, v4, v29, s16
	v_add3_u32 v54, v3, v54, s16
	v_pk_fma_f32 v[30:31], v[2:3], v[72:73], v[30:31] op_sel:[1,0,0] op_sel_hi:[0,1,1]
	v_pk_fma_f32 v[32:33], v[4:5], v[42:43], v[32:33] op_sel:[1,0,0] op_sel_hi:[0,1,1]
	v_pk_fma_f32 v[34:35], v[2:3], v[44:45], v[34:35] op_sel:[1,0,0] op_sel_hi:[0,1,1]
	v_pk_fma_f32 v[36:37], v[4:5], v[58:59], v[36:37] op_sel:[1,0,0] op_sel_hi:[0,1,1]
	v_pk_fma_f32 v[38:39], v[2:3], v[60:61], v[38:39] op_sel:[1,0,0] op_sel_hi:[0,1,1]
	v_pk_fma_f32 v[40:41], v[4:5], v[74:75], v[40:41] op_sel:[1,0,0] op_sel_hi:[0,1,1]
	v_pk_fma_f32 v[2:3], v[2:3], v[82:83], v[46:47] op_sel_hi:[1,1,0]
	v_pk_fma_f32 v[4:5], v[4:5], v[84:85], v[48:49] op_sel_hi:[1,1,0]
	v_pk_mov_b32 v[42:43], v[52:53], v[50:51] op_sel:[1,0]
	v_mov_b32_e32 v53, v51
	v_and_b32_e32 v3, 0xffff0000, v49
	v_and_b32_e32 v5, 0xffff0000, v54
	v_pk_add_f32 v[30:31], v[30:31], v[32:33]
	v_pk_add_f32 v[32:33], v[34:35], v[36:37]
	v_pk_add_f32 v[36:37], v[42:43], v[52:53]
	v_pk_add_f32 v[34:35], v[38:39], v[40:41]
	v_or_b32_sdwa v39, v3, v29 dst_sel:DWORD dst_unused:UNUSED_PAD src0_sel:DWORD src1_sel:WORD_1
	v_or_b32_sdwa v38, v5, v47 dst_sel:DWORD dst_unused:UNUSED_PAD src0_sel:DWORD src1_sel:WORD_1
	v_mov_b32_e32 v3, v36
	v_mov_b32_e32 v5, v37
	v_pk_add_f32 v[2:3], v[2:3], v[4:5]
	v_pk_add_f32 v[26:27], v[26:27], v[30:31]
	v_pk_add_f32 v[24:25], v[24:25], v[32:33]
	v_pk_add_f32 v[18:19], v[18:19], v[34:35]
	global_store_dwordx2 v[22:23], v[38:39], off offset:512
	v_lshl_add_u64 v[22:23], v[22:23], 0, s[36:37]
	v_pk_add_f32 v[16:17], v[16:17], v[2:3]
	v_add_u32_e32 v29, s17, v28
	v_add_u32_e32 v90, s17, v1
	v_add_u32_e32 v98, 0x10000, v29
	v_add_u32_e32 v94, 0x12000, v29
	v_add_u32_e32 v102, 0x12400, v29
	ds_read_b128 v[30:33], v90
	ds_read_b128 v[34:37], v90 offset:1024
	ds_read_b128 v[38:41], v90 offset:8192
	ds_read_b128 v[42:45], v90 offset:9216
	ds_read_b128 v[46:49], v90 offset:16384
	ds_read_b128 v[50:53], v90 offset:17408
	ds_read_b128 v[54:57], v90 offset:24576
	ds_read_b128 v[58:61], v90 offset:25600
	ds_read_b128 v[62:65], v90 offset:32768
	ds_read_b128 v[66:69], v90 offset:33792
	ds_read_b128 v[70:73], v90 offset:40960
	ds_read_b128 v[74:77], v90 offset:41984
	ds_read_b128 v[78:81], v90 offset:49152
	ds_read_b128 v[82:85], v90 offset:50176
	ds_read_b128 v[86:89], v90 offset:57344
	ds_read_b128 v[90:93], v90 offset:58368
	v_add_u32_e32 v29, 0x10400, v29
	ds_read_b128 v[94:97], v94
	ds_read_b128 v[98:101], v98
	ds_read_b128 v[102:105], v102
	ds_read_b128 v[106:109], v29
	s_waitcnt lgkmcnt(14)
	v_pk_mov_b32 v[110:111], v[30:31], v[38:39] op_sel:[1,0]
	v_mov_b32_e32 v31, v39
	v_pk_mov_b32 v[38:39], v[32:33], v[40:41] op_sel:[1,0]
	v_mov_b32_e32 v33, v41
	s_waitcnt lgkmcnt(13)
	v_pk_mov_b32 v[40:41], v[46:47], v[54:55] op_sel:[1,0]
	v_mov_b32_e32 v47, v55
	v_pk_mov_b32 v[54:55], v[48:49], v[56:57] op_sel:[1,0]
	v_mov_b32_e32 v49, v57
	s_waitcnt lgkmcnt(9)
	v_pk_mov_b32 v[56:57], v[62:63], v[70:71] op_sel:[1,0]
	v_mov_b32_e32 v63, v71
	v_pk_mov_b32 v[70:71], v[64:65], v[72:73] op_sel:[1,0]
	v_mov_b32_e32 v65, v73
	v_pk_mov_b32 v[72:73], v[34:35], v[42:43] op_sel:[1,0]
	v_mov_b32_e32 v35, v43
	v_pk_mov_b32 v[42:43], v[36:37], v[44:45] op_sel:[1,0]
	v_mov_b32_e32 v37, v45
	v_pk_mov_b32 v[44:45], v[50:51], v[58:59] op_sel:[1,0]
	v_mov_b32_e32 v51, v59
	v_pk_mov_b32 v[58:59], v[52:53], v[60:61] op_sel:[1,0]
	v_mov_b32_e32 v53, v61
	s_waitcnt lgkmcnt(8)
	v_pk_mov_b32 v[60:61], v[66:67], v[74:75] op_sel:[1,0]
	v_mov_b32_e32 v67, v75
	v_pk_mov_b32 v[74:75], v[68:69], v[76:77] op_sel:[1,0]
	v_mov_b32_e32 v69, v77
	s_addk_i32 s17, 0x800
	s_waitcnt vmcnt(7) lgkmcnt(2)
	v_pk_fma_f32 v[96:97], v[138:139], v[96:97], v[100:101]
	v_pk_fma_f32 v[94:95], v[136:137], v[94:95], v[98:99]
	v_and_b32_sdwa v5, v97, v6 dst_sel:DWORD dst_unused:UNUSED_PAD src0_sel:WORD_1 src1_sel:DWORD
	v_and_b32_sdwa v3, v95, v6 dst_sel:DWORD dst_unused:UNUSED_PAD src0_sel:WORD_1 src1_sel:DWORD
	v_and_b32_sdwa v2, v94, v6 dst_sel:DWORD dst_unused:UNUSED_PAD src0_sel:WORD_1 src1_sel:DWORD
	v_and_b32_sdwa v4, v96, v6 dst_sel:DWORD dst_unused:UNUSED_PAD src0_sel:WORD_1 src1_sel:DWORD
	v_add3_u32 v3, v95, v3, s16
	v_add3_u32 v5, v97, v5, s16
	v_add3_u32 v2, v94, v2, s16
	v_add3_u32 v4, v96, v4, s16
	v_and_b32_e32 v5, 0xffff0000, v5
	v_and_b32_e32 v29, 0xffff0000, v3
	v_or_b32_sdwa v3, v5, v4 dst_sel:DWORD dst_unused:UNUSED_PAD src0_sel:DWORD src1_sel:WORD_1
	v_or_b32_sdwa v2, v29, v2 dst_sel:DWORD dst_unused:UNUSED_PAD src0_sel:DWORD src1_sel:WORD_1
	global_store_dwordx2 v[22:23], v[2:3], off
	v_pk_mul_f32 v[30:31], v[94:95], v[30:31]
	v_pk_mul_f32 v[32:33], v[96:97], v[32:33]
	v_pk_mul_f32 v[46:47], v[94:95], v[46:47]
	v_pk_mul_f32 v[48:49], v[96:97], v[48:49]
	v_pk_mul_f32 v[88:89], v[96:97], v[88:89]
	v_pk_mul_f32 v[86:87], v[94:95], v[86:87]
	v_mul_f32_e32 v76, v95, v79
	v_mul_f32_e32 v98, v97, v81
	v_pk_fma_f32 v[30:31], v[94:95], v[110:111], v[30:31] op_sel:[1,0,0] op_sel_hi:[0,1,1]
	v_pk_fma_f32 v[40:41], v[94:95], v[40:41], v[46:47] op_sel:[1,0,0] op_sel_hi:[0,1,1]
	v_pk_fma_f32 v[32:33], v[96:97], v[38:39], v[32:33] op_sel:[1,0,0] op_sel_hi:[0,1,1]
	v_pk_fma_f32 v[38:39], v[96:97], v[54:55], v[48:49] op_sel:[1,0,0] op_sel_hi:[0,1,1]
	v_pk_mov_b32 v[54:55], v[86:87], v[88:89] op_sel:[1,0]
	v_mov_b32_e32 v87, v89
	v_pk_mul_f32 v[62:63], v[94:95], v[62:63]
	v_pk_mul_f32 v[64:65], v[96:97], v[64:65]
	v_pk_fma_f32 v[76:77], v[94:95], v[78:79], v[76:77] op_sel_hi:[1,1,0]
	v_pk_fma_f32 v[78:79], v[96:97], v[80:81], v[98:99] op_sel_hi:[1,1,0]
	v_pk_add_f32 v[30:31], v[30:31], v[32:33]
	v_pk_add_f32 v[32:33], v[40:41], v[38:39]
	v_pk_add_f32 v[40:41], v[54:55], v[86:87]
	v_pk_fma_f32 v[46:47], v[94:95], v[56:57], v[62:63] op_sel:[1,0,0] op_sel_hi:[0,1,1]
	v_pk_fma_f32 v[48:49], v[96:97], v[70:71], v[64:65] op_sel:[1,0,0] op_sel_hi:[0,1,1]
	v_mov_b32_e32 v77, v40
	v_mov_b32_e32 v79, v41
	v_pk_add_f32 v[38:39], v[46:47], v[48:49]
	v_pk_add_f32 v[26:27], v[26:27], v[30:31]
	v_pk_add_f32 v[30:31], v[76:77], v[78:79]
	v_pk_add_f32 v[24:25], v[24:25], v[32:33]
	v_pk_add_f32 v[18:19], v[18:19], v[38:39]
	v_pk_add_f32 v[16:17], v[16:17], v[30:31]
	v_lshl_add_u64 v[20:21], v[20:21], 0, s[40:41]
	s_waitcnt vmcnt(7) lgkmcnt(0)
	v_pk_fma_f32 v[4:5], v[142:143], v[104:105], v[108:109]
	v_pk_fma_f32 v[2:3], v[140:141], v[102:103], v[106:107]
	v_and_b32_sdwa v49, v5, v6 dst_sel:DWORD dst_unused:UNUSED_PAD src0_sel:WORD_1 src1_sel:DWORD
	v_and_b32_sdwa v47, v2, v6 dst_sel:DWORD dst_unused:UNUSED_PAD src0_sel:WORD_1 src1_sel:DWORD
	v_and_b32_sdwa v29, v4, v6 dst_sel:DWORD dst_unused:UNUSED_PAD src0_sel:WORD_1 src1_sel:DWORD
	v_and_b32_sdwa v54, v3, v6 dst_sel:DWORD dst_unused:UNUSED_PAD src0_sel:WORD_1 src1_sel:DWORD
	v_pk_mul_f32 v[30:31], v[2:3], v[34:35]
	v_pk_mul_f32 v[32:33], v[4:5], v[36:37]
	v_pk_mul_f32 v[34:35], v[2:3], v[50:51]
	v_pk_mul_f32 v[36:37], v[4:5], v[52:53]
	v_pk_mul_f32 v[38:39], v[2:3], v[66:67]
	v_pk_mul_f32 v[40:41], v[4:5], v[68:69]
	v_mul_f32_e32 v46, v3, v83
	v_mul_f32_e32 v48, v5, v85
	v_pk_mul_f32 v[50:51], v[4:5], v[92:93]
	v_pk_mul_f32 v[52:53], v[2:3], v[90:91]
	v_add3_u32 v47, v2, v47, s16
	v_add3_u32 v49, v5, v49, s16
	v_add3_u32 v29, v4, v29, s16
	v_add3_u32 v54, v3, v54, s16
	v_pk_fma_f32 v[30:31], v[2:3], v[72:73], v[30:31] op_sel:[1,0,0] op_sel_hi:[0,1,1]
	v_pk_fma_f32 v[32:33], v[4:5], v[42:43], v[32:33] op_sel:[1,0,0] op_sel_hi:[0,1,1]
	v_pk_fma_f32 v[34:35], v[2:3], v[44:45], v[34:35] op_sel:[1,0,0] op_sel_hi:[0,1,1]
	v_pk_fma_f32 v[36:37], v[4:5], v[58:59], v[36:37] op_sel:[1,0,0] op_sel_hi:[0,1,1]
	v_pk_fma_f32 v[38:39], v[2:3], v[60:61], v[38:39] op_sel:[1,0,0] op_sel_hi:[0,1,1]
	v_pk_fma_f32 v[40:41], v[4:5], v[74:75], v[40:41] op_sel:[1,0,0] op_sel_hi:[0,1,1]
	v_pk_fma_f32 v[2:3], v[2:3], v[82:83], v[46:47] op_sel_hi:[1,1,0]
	v_pk_fma_f32 v[4:5], v[4:5], v[84:85], v[48:49] op_sel_hi:[1,1,0]
	v_pk_mov_b32 v[42:43], v[52:53], v[50:51] op_sel:[1,0]
	v_mov_b32_e32 v53, v51
	v_and_b32_e32 v3, 0xffff0000, v49
	v_and_b32_e32 v5, 0xffff0000, v54
	v_pk_add_f32 v[30:31], v[30:31], v[32:33]
	v_pk_add_f32 v[32:33], v[34:35], v[36:37]
	v_pk_add_f32 v[36:37], v[42:43], v[52:53]
	v_pk_add_f32 v[34:35], v[38:39], v[40:41]
	v_or_b32_sdwa v39, v3, v29 dst_sel:DWORD dst_unused:UNUSED_PAD src0_sel:DWORD src1_sel:WORD_1
	v_or_b32_sdwa v38, v5, v47 dst_sel:DWORD dst_unused:UNUSED_PAD src0_sel:DWORD src1_sel:WORD_1
	v_mov_b32_e32 v3, v36
	v_mov_b32_e32 v5, v37
	v_pk_add_f32 v[2:3], v[2:3], v[4:5]
	v_pk_add_f32 v[26:27], v[26:27], v[30:31]
	v_pk_add_f32 v[24:25], v[24:25], v[32:33]
	v_pk_add_f32 v[18:19], v[18:19], v[34:35]
	global_store_dwordx2 v[22:23], v[38:39], off offset:512
	v_lshl_add_u64 v[22:23], v[22:23], 0, s[36:37]
	v_pk_add_f32 v[16:17], v[16:17], v[2:3]
	v_add_f32_dpp v2, v26, v26 quad_perm:[1,0,3,2] row_mask:0xf bank_mask:0xf bound_ctrl:1
	v_add_f32_dpp v4, v27, v27 quad_perm:[1,0,3,2] row_mask:0xf bank_mask:0xf bound_ctrl:1
	v_add_f32_dpp v20, v24, v24 quad_perm:[1,0,3,2] row_mask:0xf bank_mask:0xf bound_ctrl:1
	v_add_f32_dpp v2, v2, v2 quad_perm:[2,3,0,1] row_mask:0xf bank_mask:0xf bound_ctrl:1
	v_add_f32_dpp v4, v4, v4 quad_perm:[2,3,0,1] row_mask:0xf bank_mask:0xf bound_ctrl:1
	v_add_f32_dpp v20, v20, v20 quad_perm:[2,3,0,1] row_mask:0xf bank_mask:0xf bound_ctrl:1
	v_add_f32_dpp v2, v2, v2 row_half_mirror row_mask:0xf bank_mask:0xf bound_ctrl:1
	v_add_f32_dpp v4, v4, v4 row_half_mirror row_mask:0xf bank_mask:0xf bound_ctrl:1
	v_add_f32_dpp v20, v20, v20 row_half_mirror row_mask:0xf bank_mask:0xf bound_ctrl:1
	v_add_f32_dpp v2, v2, v2 row_mirror row_mask:0xf bank_mask:0xf bound_ctrl:1
	v_mov_b32_e32 v3, v2
	v_add_f32_dpp v4, v4, v4 row_mirror row_mask:0xf bank_mask:0xf bound_ctrl:1
	s_nop 0
	v_permlane16_swap_b32_e32 v2, v3
	v_add_f32_e32 v2, v2, v3
	v_mov_b32_e32 v3, v2
	v_mov_b32_e32 v5, v4
	v_add_f32_dpp v20, v20, v20 row_mirror row_mask:0xf bank_mask:0xf bound_ctrl:1
	s_nop 0
	v_permlane16_swap_b32_e32 v4, v5
	v_add_f32_e32 v4, v4, v5
	v_mov_b32_e32 v5, v4
	v_mov_b32_e32 v21, v20
	v_add_f32_dpp v22, v25, v25 quad_perm:[1,0,3,2] row_mask:0xf bank_mask:0xf bound_ctrl:1
	v_add_f32_dpp v18, v18, v18 quad_perm:[1,0,3,2] row_mask:0xf bank_mask:0xf bound_ctrl:1
	v_permlane16_swap_b32_e32 v20, v21
	v_add_f32_dpp v22, v22, v22 quad_perm:[2,3,0,1] row_mask:0xf bank_mask:0xf bound_ctrl:1
	v_add_f32_e32 v20, v20, v21
	v_mov_b32_e32 v21, v20
	v_add_f32_dpp v22, v22, v22 row_half_mirror row_mask:0xf bank_mask:0xf bound_ctrl:1
	v_add_f32_dpp v18, v18, v18 quad_perm:[2,3,0,1] row_mask:0xf bank_mask:0xf bound_ctrl:1
	v_add_f32_dpp v19, v19, v19 quad_perm:[1,0,3,2] row_mask:0xf bank_mask:0xf bound_ctrl:1
	v_add_f32_dpp v22, v22, v22 row_mirror row_mask:0xf bank_mask:0xf bound_ctrl:1
	v_mov_b32_e32 v23, v22
	v_add_f32_dpp v18, v18, v18 row_half_mirror row_mask:0xf bank_mask:0xf bound_ctrl:1
	s_nop 0
	v_permlane16_swap_b32_e32 v22, v23
	v_add_f32_e32 v22, v22, v23
	v_add_f32_dpp v18, v18, v18 row_mirror row_mask:0xf bank_mask:0xf bound_ctrl:1
	v_mov_b32_e32 v23, v22
	v_mov_b32_e32 v24, v18
	v_add_f32_dpp v19, v19, v19 quad_perm:[2,3,0,1] row_mask:0xf bank_mask:0xf bound_ctrl:1
	s_nop 0
	v_permlane16_swap_b32_e32 v18, v24
	v_add_f32_dpp v19, v19, v19 row_half_mirror row_mask:0xf bank_mask:0xf bound_ctrl:1
	v_add_f32_e32 v18, v18, v24
	v_mov_b32_e32 v24, v18
	v_add_f32_dpp v19, v19, v19 row_mirror row_mask:0xf bank_mask:0xf bound_ctrl:1
	v_mov_b32_e32 v25, v19
	v_add_f32_dpp v16, v16, v16 quad_perm:[1,0,3,2] row_mask:0xf bank_mask:0xf bound_ctrl:1
	v_add_f32_dpp v17, v17, v17 quad_perm:[1,0,3,2] row_mask:0xf bank_mask:0xf bound_ctrl:1
	v_permlane16_swap_b32_e32 v19, v25
	v_add_f32_dpp v16, v16, v16 quad_perm:[2,3,0,1] row_mask:0xf bank_mask:0xf bound_ctrl:1
	v_add_f32_e32 v19, v19, v25
	v_mov_b32_e32 v25, v19
	v_add_f32_dpp v16, v16, v16 row_half_mirror row_mask:0xf bank_mask:0xf bound_ctrl:1
	v_add_f32_dpp v17, v17, v17 quad_perm:[2,3,0,1] row_mask:0xf bank_mask:0xf bound_ctrl:1
	v_permlane32_swap_b32_e32 v2, v3
	v_add_f32_dpp v16, v16, v16 row_mirror row_mask:0xf bank_mask:0xf bound_ctrl:1
	v_mov_b32_e32 v26, v16
	v_add_f32_dpp v17, v17, v17 row_half_mirror row_mask:0xf bank_mask:0xf bound_ctrl:1
	s_nop 0
	v_permlane16_swap_b32_e32 v16, v26
	v_add_f32_e32 v16, v16, v26
	v_add_f32_dpp v17, v17, v17 row_mirror row_mask:0xf bank_mask:0xf bound_ctrl:1
	v_mov_b32_e32 v26, v16
	v_mov_b32_e32 v27, v17
	v_permlane32_swap_b32_e32 v4, v5
	s_nop 0
	v_permlane16_swap_b32_e32 v17, v27
	v_add_f32_e32 v17, v17, v27
	v_mov_b32_e32 v27, v17
	v_permlane32_swap_b32_e32 v20, v21
	v_permlane32_swap_b32_e32 v22, v23
	v_permlane32_swap_b32_e32 v18, v24
	v_permlane32_swap_b32_e32 v19, v25
	v_permlane32_swap_b32_e32 v16, v26
	v_permlane32_swap_b32_e32 v17, v27
	s_and_saveexec_b64 s[42:43], vcc
	s_cbranch_execz .LBB0_110
	global_load_dword v28, v[8:9], off
	v_add_f32_e32 v4, v4, v5
	v_add_f32_e32 v2, v2, v3
	v_add_f32_e32 v20, v20, v21
	v_cndmask_b32_e64 v2, v2, v4, s[2:3]
	v_add_f32_e32 v22, v22, v23
	v_cndmask_b32_e64 v2, v2, v20, s[4:5]
	v_add_f32_e32 v18, v18, v24
	v_cndmask_b32_e64 v2, v2, v22, s[6:7]
	v_add_f32_e32 v19, v19, v25
	v_cndmask_b32_e64 v2, v2, v18, s[8:9]
	v_add_f32_e32 v16, v16, v26
	v_cndmask_b32_e64 v2, v2, v19, s[10:11]
	v_add_f32_e32 v17, v17, v27
	v_cndmask_b32_e64 v2, v2, v16, s[12:13]
	s_lshl_b64 s[20:21], s[28:29], 5
	v_cndmask_b32_e64 v2, v2, v17, s[14:15]
	s_waitcnt vmcnt(0)
	v_add_f32_e32 v4, v2, v28
	v_lshl_add_u64 v[2:3], v[10:11], 0, s[20:21]
	global_store_dword v[2:3], v4, off
	s_branch .LBB0_110
